# speedup vs baseline: 1.0294x; 1.0066x over previous
.LBB6_4:
	s_load_dwordx2 s[2:3], s[0:1], 0x14
	s_lshl_b32 s12, s15, 7
	s_lshl_b32 s13, s14, 6
	v_lshrrev_b32_e32 v2, 4, v0
	v_xor_b32_e32 v1, v2, v0
	s_waitcnt lgkmcnt(0)
	v_and_b32_e32 v76, 15, v0
	v_lshrrev_b32_e32 v77, 7, v0
	v_lshl_or_b32 v76, v77, 5, v76
	v_or_b32_e32 v76, s12, v76
	v_bfe_u32 v77, v0, 4, 2
	v_bfe_u32 v78, v0, 6, 1
	v_lshlrev_b32_e32 v77, 2, v77
	v_lshl_or_b32 v77, v78, 5, v77
	v_or_b32_e32 v77, s13, v77
	v_mul_lo_u32 v78, v76, s2
	s_lshl_b32 s22, s2, 6
	v_add_lshl_u32 v78, v78, v77, 2
	v_lshlrev_b32_e32 v77, 2, v77
	v_add_u32_e32 v79, s22, v78
	global_load_dwordx4 v[80:83], v78, s[8:9]
	global_load_dwordx4 v[84:87], v78, s[8:9] offset:64
	global_load_dwordx4 v[88:91], v77, s[10:11]
	global_load_dwordx4 v[92:95], v77, s[10:11] offset:64
	global_load_dwordx4 v[96:99], v79, s[8:9]
	global_load_dwordx4 v[100:103], v79, s[8:9] offset:64
	s_ashr_i32 s14, s3, 31
	s_mul_i32 s0, s12, s14
	s_mul_hi_u32 s1, s12, s3
	s_add_i32 s1, s1, s0
	s_mul_i32 s0, s12, s3
	v_or_b32_e32 v4, 0x200, v0
	s_lshl_b64 s[0:1], s[0:1], 1
	v_lshlrev_b32_e32 v1, 3, v1
	v_lshrrev_b32_e32 v3, 3, v0
	v_lshrrev_b32_e32 v4, 3, v4
	s_add_u32 s0, s4, s0
	v_and_b32_e32 v1, 56, v1
	v_mul_lo_u32 v3, v3, s3
	v_mul_lo_u32 v4, v4, s3
	s_addc_u32 s1, s5, s1
	s_mul_i32 s4, s13, s14
	s_mul_hi_u32 s5, s13, s3
	v_lshlrev_b32_e32 v54, 4, v0
	v_add_lshl_u32 v3, v3, v1, 1
	v_add_lshl_u32 v4, v4, v1, 1
	s_add_i32 s5, s5, s4
	s_mul_i32 s4, s13, s3
	v_add_u32_e32 v1, 0, v54
	s_lshl_b64 s[4:5], s[4:5], 1
	v_readfirstlane_b32 s19, v1
	v_add_u32_e32 v5, 0x2000, v1
	s_add_u32 s4, s6, s4
	s_mov_b32 m0, s19
	v_readfirstlane_b32 s17, v5
	v_add_u32_e32 v5, 0x4000, v1
	s_addc_u32 s5, s7, s5
	global_load_lds_dwordx4 v3, s[0:1]
	s_mov_b32 m0, s17
	v_readfirstlane_b32 s18, v5
	v_add_u32_e32 v5, 0x6000, v1
	global_load_lds_dwordx4 v4, s[0:1]
	s_mov_b32 m0, s18
	s_add_u32 s6, s0, 0x80
	v_readfirstlane_b32 s16, v5
	v_add_u32_e32 v5, 0x8000, v1
	global_load_lds_dwordx4 v3, s[4:5]
	s_addc_u32 s7, s1, 0
	s_mov_b32 m0, s16
	v_readfirstlane_b32 s14, v5
	v_add_u32_e32 v5, 0xa000, v1
	s_add_u32 s20, s4, 0x80
	global_load_lds_dwordx4 v3, s[6:7]
	s_mov_b32 m0, s14
	v_readfirstlane_b32 s15, v5
	s_addc_u32 s21, s5, 0
	global_load_lds_dwordx4 v4, s[6:7]
	s_mov_b32 m0, s15
	v_add_u32_e32 v5, 0xc000, v1
	global_load_lds_dwordx4 v3, s[20:21]
	s_add_u32 s20, s0, 0x100
	s_addc_u32 s21, s1, 0
	v_readfirstlane_b32 s7, v5
	v_add_u32_e32 v5, 0xe000, v1
	s_add_u32 s22, s4, 0x100
	s_mov_b32 m0, s7
	v_readfirstlane_b32 s3, v5
	v_add_u32_e32 v5, 0x10000, v1
	s_addc_u32 s23, s5, 0
	global_load_lds_dwordx4 v3, s[20:21]
	s_mov_b32 m0, s3
	v_readfirstlane_b32 s6, v5
	v_add_u32_e32 v5, 0x12000, v1
	global_load_lds_dwordx4 v4, s[20:21]
	s_mov_b32 m0, s6
	s_add_u32 s20, s0, 0x180
	v_readfirstlane_b32 s24, v5
	v_add_u32_e32 v5, 0x14000, v1
	global_load_lds_dwordx4 v3, s[22:23]
	s_addc_u32 s21, s1, 0
	s_mov_b32 m0, s24
	v_readfirstlane_b32 s24, v5
	s_add_u32 s22, s4, 0x180
	global_load_lds_dwordx4 v3, s[20:21]
	s_mov_b32 m0, s24
	v_add_u32_e32 v5, 0x16000, v1
	s_addc_u32 s23, s5, 0
	global_load_lds_dwordx4 v4, s[20:21]
	v_readfirstlane_b32 s20, v5
	v_add_u32_e32 v5, 0x18000, v1
	s_mov_b32 m0, s20
	s_add_u32 s20, s0, 0x200
	v_readfirstlane_b32 s24, v5
	v_add_u32_e32 v5, 0x1a000, v1
	global_load_lds_dwordx4 v3, s[22:23]
	s_addc_u32 s21, s1, 0
	s_mov_b32 m0, s24
	v_readfirstlane_b32 s24, v5
	s_add_u32 s22, s4, 0x200
	global_load_lds_dwordx4 v3, s[20:21]
	s_mov_b32 m0, s24
	v_add_u32_e32 v5, 0x1c000, v1
	s_addc_u32 s23, s5, 0
	global_load_lds_dwordx4 v4, s[20:21]
	v_readfirstlane_b32 s20, v5
	v_add_u32_e32 v5, 0x1e000, v1
	s_mov_b32 m0, s20
	s_add_u32 s20, s0, 0x280
	v_readfirstlane_b32 s24, v5
	v_add_u32_e32 v5, 0x20000, v1
	global_load_lds_dwordx4 v3, s[22:23]
	s_addc_u32 s21, s1, 0
	s_mov_b32 m0, s24
	v_readfirstlane_b32 s24, v5
	global_load_lds_dwordx4 v3, s[20:21]
	s_mov_b32 m0, s24
	v_add_u32_e32 v1, 0x22000, v1
	s_add_u32 s22, s4, 0x280
	global_load_lds_dwordx4 v4, s[20:21]
	v_readfirstlane_b32 s20, v1
	s_addc_u32 s23, s5, 0
	s_mov_b32 m0, s20
	v_bfe_u32 v7, v0, 1, 3
	global_load_lds_dwordx4 v3, s[22:23]
	v_lshrrev_b32_e32 v6, 1, v0
	v_bitop3_b32 v2, v2, v7, 3 bitop3:0x6c
	v_and_b32_e32 v5, 15, v0
	v_lshrrev_b32_e32 v1, 2, v0
	s_movk_i32 s20, 0x60
	v_lshlrev_b32_e32 v9, 4, v2
	v_and_b32_e32 v2, 32, v6
	v_and_or_b32 v1, v1, s20, v5
	v_or_b32_e32 v5, v2, v5
	v_lshlrev_b32_e32 v6, 7, v5
	v_add_u32_e32 v38, 0, v6
	s_waitcnt vmcnt(15)
	s_barrier
	v_add_u32_e32 v8, v38, v9
	ds_read_b128 v[10:13], v8 offset:16384
	v_lshlrev_b32_e32 v55, 7, v1
	v_add_u32_e32 v30, 0, v55
	v_add_u32_e32 v5, v30, v9
	ds_read_b128 v[14:17], v5
	ds_read_b128 v[18:21], v8 offset:18432
	ds_read_b128 v[22:25], v5 offset:2048
	v_bfe_u32 v0, v0, 4, 2
	v_bitop3_b32 v9, v0, v7, 4 bitop3:0x36
	s_waitcnt lgkmcnt(0)
	v_mfma_f32_16x16x32_f16 v[26:29], v[10:13], v[14:17], 0
	v_or_b32_e32 v56, 0x4000, v6
	v_add_u32_e32 v7, 0x4000, v8
	v_lshlrev_b32_e32 v57, 4, v9
	v_mfma_f32_16x16x32_f16 v[14:17], v[18:21], v[14:17], 0
	v_add_u32_e32 v6, v30, v57
	v_add_u32_e32 v9, v38, v57
	ds_read_b128 v[30:33], v6
	ds_read_b128 v[34:37], v6 offset:2048
	ds_read_b128 v[38:41], v9 offset:16384
	ds_read_b128 v[42:45], v9 offset:18432
	v_mfma_f32_16x16x32_f16 v[10:13], v[10:13], v[22:25], 0
	v_mfma_f32_16x16x32_f16 v[18:21], v[18:21], v[22:25], 0
	s_add_u32 s20, s0, 0x300
	s_mov_b32 m0, s19
	s_waitcnt vmcnt(12) lgkmcnt(0)
	s_barrier
	s_addc_u32 s21, s1, 0
	s_add_u32 s22, s4, 0x300
	global_load_lds_dwordx4 v3, s[20:21]
	s_mov_b32 m0, s17
	s_addc_u32 s23, s5, 0
	global_load_lds_dwordx4 v4, s[20:21]
	s_mov_b32 m0, s18
	s_nop 0
	global_load_lds_dwordx4 v3, s[22:23]
	s_waitcnt lgkmcnt(0)
	v_mfma_f32_16x16x32_f16 v[22:25], v[38:41], v[30:33], v[26:29]
	v_mfma_f32_16x16x32_f16 v[14:17], v[42:45], v[30:33], v[14:17]
	s_nop 1
	ds_read_b128 v[26:29], v5 offset:24576
	ds_read_b128 v[30:33], v5 offset:26624
	ds_read_b128 v[46:49], v8 offset:40960
	ds_read_b128 v[50:53], v8 offset:43008
	v_mfma_f32_16x16x32_f16 v[10:13], v[38:41], v[34:37], v[10:13]
	v_mfma_f32_16x16x32_f16 v[18:21], v[42:45], v[34:37], v[18:21]
	s_waitcnt lgkmcnt(0)
	v_mfma_f32_16x16x32_f16 v[22:25], v[46:49], v[26:29], v[22:25]
	v_mfma_f32_16x16x32_f16 v[14:17], v[50:53], v[26:29], v[14:17]
	ds_read_b128 v[26:29], v6 offset:24576
	ds_read_b128 v[34:37], v6 offset:26624
	ds_read_b128 v[38:41], v9 offset:40960
	ds_read_b128 v[42:45], v9 offset:43008
	v_mfma_f32_16x16x32_f16 v[10:13], v[46:49], v[30:33], v[10:13]
	v_mfma_f32_16x16x32_f16 v[18:21], v[50:53], v[30:33], v[18:21]
	s_add_u32 s20, s0, 0x380
	s_mov_b32 m0, s16
	s_waitcnt vmcnt(12) lgkmcnt(0)
	s_barrier
	s_addc_u32 s21, s1, 0
	s_add_u32 s22, s4, 0x380
	global_load_lds_dwordx4 v3, s[20:21]
	s_mov_b32 m0, s14
	s_addc_u32 s23, s5, 0
	global_load_lds_dwordx4 v4, s[20:21]
	s_mov_b32 m0, s15
	s_nop 0
	global_load_lds_dwordx4 v3, s[22:23]
	s_waitcnt lgkmcnt(0)
	v_mfma_f32_16x16x32_f16 v[22:25], v[38:41], v[26:29], v[22:25]
	v_mfma_f32_16x16x32_f16 v[14:17], v[42:45], v[26:29], v[14:17]
	ds_read_b128 v[26:29], v5 offset:49152
	ds_read_b128 v[30:33], v5 offset:51200
	ds_read_b128 v[46:49], v7 offset:49152
	ds_read_b128 v[50:53], v7 offset:51200
	v_mfma_f32_16x16x32_f16 v[10:13], v[38:41], v[34:37], v[10:13]
	v_mfma_f32_16x16x32_f16 v[18:21], v[42:45], v[34:37], v[18:21]
	s_waitcnt lgkmcnt(0)
	v_mfma_f32_16x16x32_f16 v[22:25], v[46:49], v[26:29], v[22:25]
	v_mfma_f32_16x16x32_f16 v[14:17], v[50:53], v[26:29], v[14:17]
	s_add_i32 s20, 0, 0xc000
	v_add3_u32 v58, s20, v57, v56
	ds_read_b128 v[26:29], v6 offset:49152
	ds_read_b128 v[34:37], v6 offset:51200
	ds_read_b128 v[38:41], v58
	ds_read_b128 v[42:45], v58 offset:2048
	v_mfma_f32_16x16x32_f16 v[10:13], v[46:49], v[30:33], v[10:13]
	v_mfma_f32_16x16x32_f16 v[18:21], v[50:53], v[30:33], v[18:21]
	s_add_u32 s20, s0, 0x400
	s_mov_b32 m0, s7
	s_waitcnt vmcnt(12) lgkmcnt(0)
	s_barrier
	s_addc_u32 s21, s1, 0
	s_add_u32 s22, s4, 0x400
	global_load_lds_dwordx4 v3, s[20:21]
	s_mov_b32 m0, s3
	s_addc_u32 s23, s5, 0
	global_load_lds_dwordx4 v4, s[20:21]
	s_mov_b32 m0, s6
	s_nop 0
	global_load_lds_dwordx4 v3, s[22:23]
	s_waitcnt lgkmcnt(0)
	v_mfma_f32_16x16x32_f16 v[22:25], v[38:41], v[26:29], v[22:25]
	v_mfma_f32_16x16x32_f16 v[14:17], v[42:45], v[26:29], v[14:17]
	v_add_u32_e32 v59, 0x12000, v5
	v_add_u32_e32 v61, 0x16000, v8
	v_add_u32_e32 v60, 0x12800, v5
	ds_read_b128 v[26:29], v59
	ds_read_b128 v[30:33], v60
	v_add_u32_e32 v62, 0x16800, v8
	ds_read_b128 v[46:49], v61
	ds_read_b128 v[50:53], v62
	v_mfma_f32_16x16x32_f16 v[10:13], v[38:41], v[34:37], v[10:13]
	v_mfma_f32_16x16x32_f16 v[18:21], v[42:45], v[34:37], v[18:21]
	s_waitcnt lgkmcnt(0)
	v_mfma_f32_16x16x32_f16 v[22:25], v[46:49], v[26:29], v[22:25]
	v_mfma_f32_16x16x32_f16 v[14:17], v[50:53], v[26:29], v[14:17]
	s_add_i32 s20, 0, 0x12000
	v_add_u32_e32 v38, s20, v57
	v_add_u32_e32 v63, v38, v55
	v_add_u32_e32 v64, v38, v56
	ds_read_b128 v[26:29], v63
	ds_read_b128 v[34:37], v63 offset:2048
	ds_read_b128 v[38:41], v64
	ds_read_b128 v[42:45], v64 offset:2048
	v_mfma_f32_16x16x32_f16 v[10:13], v[46:49], v[30:33], v[10:13]
	v_mfma_f32_16x16x32_f16 v[18:21], v[50:53], v[30:33], v[18:21]
	v_add_u32_e32 v30, s20, v54
	s_add_u32 s24, s0, 0x480
	v_readfirstlane_b32 s22, v30
	v_add_u32_e32 v31, 0x2000, v30
	s_waitcnt vmcnt(12) lgkmcnt(0)
	s_barrier
	s_addc_u32 s25, s1, 0
	s_mov_b32 m0, s22
	v_readfirstlane_b32 s20, v31
	v_add_u32_e32 v30, 0x4000, v30
	s_add_u32 s26, s4, 0x480
	global_load_lds_dwordx4 v3, s[24:25]
	s_mov_b32 m0, s20
	v_readfirstlane_b32 s21, v30
	s_addc_u32 s27, s5, 0
	global_load_lds_dwordx4 v4, s[24:25]
	s_mov_b32 m0, s21
	s_nop 0
	global_load_lds_dwordx4 v3, s[26:27]
	s_waitcnt lgkmcnt(0)
	v_mfma_f32_16x16x32_f16 v[22:25], v[38:41], v[26:29], v[22:25]
	v_mfma_f32_16x16x32_f16 v[14:17], v[42:45], v[26:29], v[14:17]
	v_add_u32_e32 v65, 0x18000, v5
	v_add_u32_e32 v67, 0x1c000, v8
	v_add_u32_e32 v66, 0x18800, v5
	ds_read_b128 v[26:29], v65
	ds_read_b128 v[30:33], v66
	v_add_u32_e32 v68, 0x1c800, v8
	ds_read_b128 v[46:49], v67
	ds_read_b128 v[50:53], v68
	v_mfma_f32_16x16x32_f16 v[10:13], v[38:41], v[34:37], v[10:13]
	v_mfma_f32_16x16x32_f16 v[18:21], v[42:45], v[34:37], v[18:21]
	s_waitcnt lgkmcnt(0)
	v_mfma_f32_16x16x32_f16 v[22:25], v[46:49], v[26:29], v[22:25]
	v_mfma_f32_16x16x32_f16 v[14:17], v[50:53], v[26:29], v[14:17]
	s_add_i32 s23, 0, 0x18000
	v_add_u32_e32 v38, s23, v57
	v_add_u32_e32 v69, v38, v55
	v_add_u32_e32 v70, v38, v56
	ds_read_b128 v[26:29], v69
	ds_read_b128 v[34:37], v69 offset:2048
	ds_read_b128 v[38:41], v70
	ds_read_b128 v[42:45], v70 offset:2048
	v_mfma_f32_16x16x32_f16 v[10:13], v[46:49], v[30:33], v[10:13]
	v_mfma_f32_16x16x32_f16 v[18:21], v[50:53], v[30:33], v[18:21]
	v_add_u32_e32 v30, s23, v54
	s_add_u32 s24, s0, 0x500
	v_readfirstlane_b32 s23, v30
	v_add_u32_e32 v31, 0x2000, v30
	s_waitcnt vmcnt(12) lgkmcnt(0)
	s_barrier
	s_addc_u32 s25, s1, 0
	s_mov_b32 m0, s23
	v_readfirstlane_b32 s23, v31
	v_add_u32_e32 v30, 0x4000, v30
	s_add_u32 s26, s4, 0x500
	global_load_lds_dwordx4 v3, s[24:25]
	s_mov_b32 m0, s23
	v_readfirstlane_b32 s23, v30
	s_addc_u32 s27, s5, 0
	global_load_lds_dwordx4 v4, s[24:25]
	s_mov_b32 m0, s23
	s_nop 0
	global_load_lds_dwordx4 v3, s[26:27]
	s_waitcnt lgkmcnt(0)
	v_mfma_f32_16x16x32_f16 v[22:25], v[38:41], v[26:29], v[22:25]
	v_mfma_f32_16x16x32_f16 v[14:17], v[42:45], v[26:29], v[14:17]
	v_add_u32_e32 v71, 0x1e000, v5
	v_add_u32_e32 v73, 0x22000, v8
	v_add_u32_e32 v72, 0x1e800, v5
	ds_read_b128 v[26:29], v71
	ds_read_b128 v[30:33], v72
	v_add_u32_e32 v74, 0x22800, v8
	ds_read_b128 v[46:49], v73
	ds_read_b128 v[50:53], v74
	v_mfma_f32_16x16x32_f16 v[10:13], v[38:41], v[34:37], v[10:13]
	v_mfma_f32_16x16x32_f16 v[18:21], v[42:45], v[34:37], v[18:21]
	s_waitcnt lgkmcnt(0)
	v_mfma_f32_16x16x32_f16 v[22:25], v[46:49], v[26:29], v[22:25]
	v_mfma_f32_16x16x32_f16 v[14:17], v[50:53], v[26:29], v[14:17]
	s_add_i32 s23, 0, 0x1e000
	v_add_u32_e32 v38, s23, v57
	v_add_u32_e32 v55, v38, v55
	v_add_u32_e32 v56, v38, v56
	ds_read_b128 v[26:29], v55
	ds_read_b128 v[34:37], v55 offset:2048
	ds_read_b128 v[38:41], v56
	ds_read_b128 v[42:45], v56 offset:2048
	v_mfma_f32_16x16x32_f16 v[10:13], v[46:49], v[30:33], v[10:13]
	v_mfma_f32_16x16x32_f16 v[18:21], v[50:53], v[30:33], v[18:21]
	v_add_u32_e32 v30, s23, v54
	s_add_u32 s24, s0, 0x580
	v_readfirstlane_b32 s23, v30
	v_add_u32_e32 v31, 0x2000, v30
	s_waitcnt vmcnt(12) lgkmcnt(0)
	s_barrier
	s_addc_u32 s25, s1, 0
	s_mov_b32 m0, s23
	v_readfirstlane_b32 s23, v31
	v_add_u32_e32 v30, 0x4000, v30
	s_add_u32 s26, s4, 0x580
	global_load_lds_dwordx4 v3, s[24:25]
	s_mov_b32 m0, s23
	v_readfirstlane_b32 s23, v30
	s_addc_u32 s27, s5, 0
	global_load_lds_dwordx4 v4, s[24:25]
	s_mov_b32 m0, s23
	s_nop 0
	global_load_lds_dwordx4 v3, s[26:27]
	s_waitcnt lgkmcnt(0)
	v_mfma_f32_16x16x32_f16 v[22:25], v[38:41], v[26:29], v[22:25]
	v_mfma_f32_16x16x32_f16 v[14:17], v[42:45], v[26:29], v[14:17]
	ds_read_b128 v[26:29], v5
	ds_read_b128 v[30:33], v5 offset:2048
	ds_read_b128 v[46:49], v8 offset:16384
	ds_read_b128 v[50:53], v8 offset:18432
	v_mfma_f32_16x16x32_f16 v[10:13], v[38:41], v[34:37], v[10:13]
	v_mfma_f32_16x16x32_f16 v[18:21], v[42:45], v[34:37], v[18:21]
	s_waitcnt lgkmcnt(0)
	v_mfma_f32_16x16x32_f16 v[22:25], v[46:49], v[26:29], v[22:25]
	v_mfma_f32_16x16x32_f16 v[14:17], v[50:53], v[26:29], v[14:17]
	ds_read_b128 v[26:29], v6
	ds_read_b128 v[34:37], v6 offset:2048
	ds_read_b128 v[38:41], v9 offset:16384
	ds_read_b128 v[42:45], v9 offset:18432
	v_mfma_f32_16x16x32_f16 v[10:13], v[46:49], v[30:33], v[10:13]
	v_mfma_f32_16x16x32_f16 v[18:21], v[50:53], v[30:33], v[18:21]
	s_add_u32 s24, s0, 0x600
	s_mov_b32 m0, s19
	s_waitcnt vmcnt(12) lgkmcnt(0)
	s_barrier
	s_addc_u32 s25, s1, 0
	s_add_u32 s26, s4, 0x600
	global_load_lds_dwordx4 v3, s[24:25]
	s_mov_b32 m0, s17
	s_addc_u32 s27, s5, 0
	global_load_lds_dwordx4 v4, s[24:25]
	s_mov_b32 m0, s18
	s_nop 0
	global_load_lds_dwordx4 v3, s[26:27]
	s_waitcnt lgkmcnt(0)
	v_mfma_f32_16x16x32_f16 v[22:25], v[38:41], v[26:29], v[22:25]
	v_mfma_f32_16x16x32_f16 v[14:17], v[42:45], v[26:29], v[14:17]
	ds_read_b128 v[26:29], v5 offset:24576
	ds_read_b128 v[30:33], v5 offset:26624
	ds_read_b128 v[46:49], v8 offset:40960
	ds_read_b128 v[50:53], v8 offset:43008
	v_mfma_f32_16x16x32_f16 v[10:13], v[38:41], v[34:37], v[10:13]
	v_mfma_f32_16x16x32_f16 v[18:21], v[42:45], v[34:37], v[18:21]
	s_waitcnt lgkmcnt(0)
	v_mfma_f32_16x16x32_f16 v[22:25], v[46:49], v[26:29], v[22:25]
	v_mfma_f32_16x16x32_f16 v[14:17], v[50:53], v[26:29], v[14:17]
	ds_read_b128 v[26:29], v6 offset:24576
	ds_read_b128 v[34:37], v6 offset:26624
	ds_read_b128 v[38:41], v9 offset:40960
	ds_read_b128 v[42:45], v9 offset:43008
	v_mfma_f32_16x16x32_f16 v[10:13], v[46:49], v[30:33], v[10:13]
	v_mfma_f32_16x16x32_f16 v[18:21], v[50:53], v[30:33], v[18:21]
	s_mov_b32 m0, s16
	s_add_u32 s16, s0, 0x680
	s_waitcnt vmcnt(12) lgkmcnt(0)
	s_barrier
	s_addc_u32 s17, s1, 0
	s_add_u32 s18, s4, 0x680
	global_load_lds_dwordx4 v3, s[16:17]
	s_mov_b32 m0, s14
	s_addc_u32 s19, s5, 0
	global_load_lds_dwordx4 v4, s[16:17]
	s_mov_b32 m0, s15
	s_nop 0
	global_load_lds_dwordx4 v3, s[18:19]
	s_waitcnt lgkmcnt(0)
	v_mfma_f32_16x16x32_f16 v[22:25], v[38:41], v[26:29], v[22:25]
	v_mfma_f32_16x16x32_f16 v[14:17], v[42:45], v[26:29], v[14:17]
	ds_read_b128 v[26:29], v5 offset:49152
	ds_read_b128 v[30:33], v5 offset:51200
	ds_read_b128 v[46:49], v7 offset:49152
	ds_read_b128 v[50:53], v7 offset:51200
	v_mfma_f32_16x16x32_f16 v[10:13], v[38:41], v[34:37], v[10:13]
	v_mfma_f32_16x16x32_f16 v[18:21], v[42:45], v[34:37], v[18:21]
	s_waitcnt lgkmcnt(0)
	v_mfma_f32_16x16x32_f16 v[22:25], v[46:49], v[26:29], v[22:25]
	v_mfma_f32_16x16x32_f16 v[14:17], v[50:53], v[26:29], v[14:17]
	ds_read_b128 v[26:29], v6 offset:49152
	ds_read_b128 v[34:37], v6 offset:51200
	ds_read_b128 v[38:41], v58
	ds_read_b128 v[42:45], v58 offset:2048
	v_mfma_f32_16x16x32_f16 v[10:13], v[46:49], v[30:33], v[10:13]
	v_mfma_f32_16x16x32_f16 v[18:21], v[50:53], v[30:33], v[18:21]
	s_add_u32 s14, s0, 0x700
	s_mov_b32 m0, s7
	s_waitcnt vmcnt(12) lgkmcnt(0)
	s_barrier
	s_addc_u32 s15, s1, 0
	s_add_u32 s16, s4, 0x700
	global_load_lds_dwordx4 v3, s[14:15]
	s_mov_b32 m0, s3
	s_addc_u32 s17, s5, 0
	global_load_lds_dwordx4 v4, s[14:15]
	s_mov_b32 m0, s6
	s_nop 0
	global_load_lds_dwordx4 v3, s[16:17]
	s_waitcnt lgkmcnt(0)
	v_mfma_f32_16x16x32_f16 v[22:25], v[38:41], v[26:29], v[22:25]
	v_mfma_f32_16x16x32_f16 v[14:17], v[42:45], v[26:29], v[14:17]
	ds_read_b128 v[26:29], v59
	ds_read_b128 v[30:33], v60
	ds_read_b128 v[46:49], v61
	ds_read_b128 v[50:53], v62
	v_mfma_f32_16x16x32_f16 v[10:13], v[38:41], v[34:37], v[10:13]
	v_mfma_f32_16x16x32_f16 v[18:21], v[42:45], v[34:37], v[18:21]
	s_waitcnt lgkmcnt(0)
	v_mfma_f32_16x16x32_f16 v[22:25], v[46:49], v[26:29], v[22:25]
	v_mfma_f32_16x16x32_f16 v[14:17], v[50:53], v[26:29], v[14:17]
	ds_read_b128 v[26:29], v63
	ds_read_b128 v[34:37], v63 offset:2048
	ds_read_b128 v[38:41], v64
	ds_read_b128 v[42:45], v64 offset:2048
	v_mfma_f32_16x16x32_f16 v[10:13], v[46:49], v[30:33], v[10:13]
	v_mfma_f32_16x16x32_f16 v[18:21], v[50:53], v[30:33], v[18:21]
	s_add_u32 s0, s0, 0x780
	s_mov_b32 m0, s22
	s_waitcnt vmcnt(12) lgkmcnt(0)
	s_barrier
	s_addc_u32 s1, s1, 0
	s_add_u32 s4, s4, 0x780
	global_load_lds_dwordx4 v3, s[0:1]
	s_mov_b32 m0, s20
	s_addc_u32 s5, s5, 0
	global_load_lds_dwordx4 v4, s[0:1]
	s_mov_b32 m0, s21
	s_nop 0
	global_load_lds_dwordx4 v3, s[4:5]
	s_waitcnt lgkmcnt(0)
	v_mfma_f32_16x16x32_f16 v[22:25], v[38:41], v[26:29], v[22:25]
	v_mfma_f32_16x16x32_f16 v[14:17], v[42:45], v[26:29], v[14:17]
	ds_read_b128 v[26:29], v65
	ds_read_b128 v[30:33], v66
	ds_read_b128 v[46:49], v67
	ds_read_b128 v[50:53], v68
	v_mfma_f32_16x16x32_f16 v[10:13], v[38:41], v[34:37], v[10:13]
	v_mfma_f32_16x16x32_f16 v[18:21], v[42:45], v[34:37], v[18:21]
	s_waitcnt lgkmcnt(0)
	v_mfma_f32_16x16x32_f16 v[22:25], v[46:49], v[26:29], v[22:25]
	v_mfma_f32_16x16x32_f16 v[14:17], v[50:53], v[26:29], v[14:17]
	ds_read_b128 v[26:29], v69
	ds_read_b128 v[34:37], v69 offset:2048
	ds_read_b128 v[38:41], v70
	ds_read_b128 v[42:45], v70 offset:2048
	v_mfma_f32_16x16x32_f16 v[10:13], v[46:49], v[30:33], v[10:13]
	v_mfma_f32_16x16x32_f16 v[18:21], v[50:53], v[30:33], v[18:21]
	s_waitcnt vmcnt(12) lgkmcnt(0)
	s_barrier
	s_waitcnt lgkmcnt(0)
	v_mfma_f32_16x16x32_f16 v[22:25], v[38:41], v[26:29], v[22:25]
	v_mfma_f32_16x16x32_f16 v[14:17], v[42:45], v[26:29], v[14:17]
	ds_read_b128 v[26:29], v71
	ds_read_b128 v[30:33], v72
	ds_read_b128 v[46:49], v73
	ds_read_b128 v[50:53], v74
	v_mfma_f32_16x16x32_f16 v[10:13], v[38:41], v[34:37], v[10:13]
	v_mfma_f32_16x16x32_f16 v[18:21], v[42:45], v[34:37], v[18:21]
	s_waitcnt lgkmcnt(0)
	v_mfma_f32_16x16x32_f16 v[22:25], v[46:49], v[26:29], v[22:25]
	v_mfma_f32_16x16x32_f16 v[14:17], v[50:53], v[26:29], v[14:17]
	ds_read_b128 v[26:29], v55
	ds_read_b128 v[34:37], v55 offset:2048
	ds_read_b128 v[38:41], v56
	ds_read_b128 v[42:45], v56 offset:2048
	v_mfma_f32_16x16x32_f16 v[10:13], v[46:49], v[30:33], v[10:13]
	v_mfma_f32_16x16x32_f16 v[18:21], v[50:53], v[30:33], v[18:21]
	s_waitcnt vmcnt(0) lgkmcnt(0)
	s_barrier
	s_waitcnt lgkmcnt(0)
	v_mfma_f32_16x16x32_f16 v[22:25], v[38:41], v[26:29], v[22:25]
	v_mfma_f32_16x16x32_f16 v[14:17], v[42:45], v[26:29], v[14:17]
	ds_read_b128 v[26:29], v5
	ds_read_b128 v[30:33], v5 offset:2048
	ds_read_b128 v[46:49], v8 offset:16384
	ds_read_b128 v[50:53], v8 offset:18432
	v_mfma_f32_16x16x32_f16 v[10:13], v[38:41], v[34:37], v[10:13]
	v_mfma_f32_16x16x32_f16 v[18:21], v[42:45], v[34:37], v[18:21]
	s_waitcnt lgkmcnt(0)
	v_mfma_f32_16x16x32_f16 v[22:25], v[46:49], v[26:29], v[22:25]
	v_mfma_f32_16x16x32_f16 v[14:17], v[50:53], v[26:29], v[14:17]
	ds_read_b128 v[26:29], v6
	ds_read_b128 v[34:37], v6 offset:2048
	ds_read_b128 v[38:41], v9 offset:16384
	ds_read_b128 v[42:45], v9 offset:18432
	v_mfma_f32_16x16x32_f16 v[10:13], v[46:49], v[30:33], v[10:13]
	v_mfma_f32_16x16x32_f16 v[18:21], v[50:53], v[30:33], v[18:21]
	s_waitcnt vmcnt(0) lgkmcnt(0)
	s_barrier
	s_waitcnt lgkmcnt(0)
	v_mfma_f32_16x16x32_f16 v[22:25], v[38:41], v[26:29], v[22:25]
	v_mfma_f32_16x16x32_f16 v[14:17], v[42:45], v[26:29], v[14:17]
	ds_read_b128 v[26:29], v5 offset:24576
	ds_read_b128 v[30:33], v5 offset:26624
	ds_read_b128 v[46:49], v8 offset:40960
	ds_read_b128 v[50:53], v8 offset:43008
	v_mfma_f32_16x16x32_f16 v[10:13], v[38:41], v[34:37], v[10:13]
	v_mfma_f32_16x16x32_f16 v[18:21], v[42:45], v[34:37], v[18:21]
	s_waitcnt lgkmcnt(0)
	v_mfma_f32_16x16x32_f16 v[22:25], v[46:49], v[26:29], v[22:25]
	v_mfma_f32_16x16x32_f16 v[14:17], v[50:53], v[26:29], v[14:17]
	ds_read_b128 v[26:29], v6 offset:24576
	ds_read_b128 v[34:37], v6 offset:26624
	ds_read_b128 v[38:41], v9 offset:40960
	ds_read_b128 v[42:45], v9 offset:43008
	v_mfma_f32_16x16x32_f16 v[8:11], v[46:49], v[30:33], v[10:13]
	v_mfma_f32_16x16x32_f16 v[18:21], v[50:53], v[30:33], v[18:21]
	s_waitcnt vmcnt(0) lgkmcnt(0)
	s_barrier
	s_waitcnt lgkmcnt(0)
	v_mfma_f32_16x16x32_f16 v[22:25], v[38:41], v[26:29], v[22:25]
	v_mfma_f32_16x16x32_f16 v[12:15], v[42:45], v[26:29], v[14:17]
	ds_read_b128 v[26:29], v5 offset:49152
	ds_read_b128 v[30:33], v5 offset:51200
	ds_read_b128 v[46:49], v7 offset:49152
	ds_read_b128 v[50:53], v7 offset:51200
	v_mfma_f32_16x16x32_f16 v[8:11], v[38:41], v[34:37], v[8:11]
	v_mfma_f32_16x16x32_f16 v[16:19], v[42:45], v[34:37], v[18:21]
	s_waitcnt lgkmcnt(0)
	v_mfma_f32_16x16x32_f16 v[20:23], v[46:49], v[26:29], v[22:25]
	v_mfma_f32_16x16x32_f16 v[12:15], v[50:53], v[26:29], v[12:15]
	s_nop 1
	ds_read_b128 v[24:27], v6 offset:49152
	ds_read_b128 v[4:7], v6 offset:51200
	ds_read_b128 v[34:37], v58
	ds_read_b128 v[38:41], v58 offset:2048
	v_mfma_f32_16x16x32_f16 v[8:11], v[46:49], v[30:33], v[8:11]
	v_mfma_f32_16x16x32_f16 v[16:19], v[50:53], v[30:33], v[16:19]
	s_waitcnt vmcnt(0) lgkmcnt(0)
	s_barrier
	s_waitcnt lgkmcnt(0)
	v_mfma_f32_16x16x32_f16 v[20:23], v[34:37], v[24:27], v[20:23]
	v_mfma_f32_16x16x32_f16 v[12:15], v[38:41], v[24:27], v[12:15]
	ds_read_b128 v[24:27], v59
	ds_read_b128 v[28:31], v60
	ds_read_b128 v[42:45], v61
	ds_read_b128 v[46:49], v62
	v_mfma_f32_16x16x32_f16 v[8:11], v[34:37], v[4:7], v[8:11]
	v_mfma_f32_16x16x32_f16 v[4:7], v[38:41], v[4:7], v[16:19]
	s_waitcnt lgkmcnt(0)
	v_mfma_f32_16x16x32_f16 v[16:19], v[42:45], v[24:27], v[20:23]
	v_mfma_f32_16x16x32_f16 v[12:15], v[46:49], v[24:27], v[12:15]
	s_nop 1
	ds_read_b128 v[20:23], v63
	ds_read_b128 v[24:27], v63 offset:2048
	ds_read_b128 v[32:35], v64
	ds_read_b128 v[36:39], v64 offset:2048
	v_mfma_f32_16x16x32_f16 v[8:11], v[42:45], v[28:31], v[8:11]
	v_mfma_f32_16x16x32_f16 v[4:7], v[46:49], v[28:31], v[4:7]
	s_waitcnt lgkmcnt(0)
	v_mfma_f32_16x16x32_f16 v[16:19], v[32:35], v[20:23], v[16:19]
	v_mfma_f32_16x16x32_f16 v[12:15], v[36:39], v[20:23], v[12:15]
	v_mfma_f32_16x16x32_f16 v[8:11], v[32:35], v[24:27], v[8:11]
	v_mfma_f32_16x16x32_f16 v[4:7], v[36:39], v[24:27], v[4:7]
	v_or_b32_e32 v38, s12, v1
	v_lshlrev_b32_e32 v0, 2, v0
	v_or3_b32 v0, v0, v2, s13
	v_mad_u64_u32 v[2:3], s[0:1], v38, s2, 0
	s_ashr_i32 s3, s2, 31
	v_mov_b32_e32 v20, v3
	v_mad_u64_u32 v[20:21], s[0:1], v38, s3, v[20:21]
	v_mov_b32_e32 v3, v20
	v_mov_b32_e32 v1, 0
	v_lshl_add_u64 v[2:3], v[2:3], 2, s[8:9]
	v_lshlrev_b64 v[32:33], 2, v[0:1]
	v_lshl_add_u64 v[34:35], v[2:3], 0, v[32:33]
	v_lshl_add_u64 v[36:37], s[10:11], 0, v[32:33]
	v_or_b32_e32 v39, 16, v38
	v_mad_u64_u32 v[36:37], s[0:1], v39, s2, 0
	v_mov_b32_e32 v38, v37
	v_mad_u64_u32 v[38:39], s[0:1], v39, s3, v[38:39]
	v_mov_b32_e32 v37, v38
	v_lshl_add_u64 v[36:37], v[36:37], 2, s[8:9]
	v_lshl_add_u64 v[32:33], v[36:37], 0, v[32:33]
	s_waitcnt vmcnt(0)
	v_pk_add_f32 v[2:3], v[18:19], v[82:83]
	v_pk_add_f32 v[0:1], v[16:17], v[80:81]
	v_pk_add_f32 v[14:15], v[14:15], v[86:87]
	v_pk_add_f32 v[12:13], v[12:13], v[84:85]
	v_pk_add_f32 v[2:3], v[90:91], v[2:3]
	v_pk_add_f32 v[0:1], v[88:89], v[0:1]
	v_pk_add_f32 v[14:15], v[94:95], v[14:15]
	v_pk_add_f32 v[12:13], v[92:93], v[12:13]
	global_store_dwordx4 v[34:35], v[0:3], off
	global_store_dwordx4 v[34:35], v[12:15], off offset:64
	v_pk_add_f32 v[42:43], v[10:11], v[98:99]
	v_pk_add_f32 v[40:41], v[8:9], v[96:97]
	v_pk_add_f32 v[6:7], v[6:7], v[102:103]
	v_pk_add_f32 v[4:5], v[4:5], v[100:101]
	v_pk_add_f32 v[42:43], v[90:91], v[42:43]
	v_pk_add_f32 v[40:41], v[88:89], v[40:41]
	v_pk_add_f32 v[6:7], v[94:95], v[6:7]
	v_pk_add_f32 v[4:5], v[92:93], v[4:5]
	global_store_dwordx4 v[32:33], v[40:43], off
	global_store_dwordx4 v[32:33], v[4:7], off offset:64
	s_endpgm
	s_endpgm
	s_endpgm
	s_endpgm

	.amdhsa_kernel _Z5gemm8ILi64ELi4ELi6ELi1ELi1ELi16EEvPKDF16_S1_iiiPDF16_PfPKf
		.amdhsa_group_segment_fixed_size 0
		.amdhsa_private_segment_fixed_size 0
		.amdhsa_kernarg_size 312
		.amdhsa_user_sgpr_count 2
		.amdhsa_user_sgpr_dispatch_ptr 0
		.amdhsa_user_sgpr_queue_ptr 0
		.amdhsa_user_sgpr_kernarg_segment_ptr 1
		.amdhsa_user_sgpr_dispatch_id 0
		.amdhsa_user_sgpr_kernarg_preload_length 0
		.amdhsa_user_sgpr_kernarg_preload_offset 0
		.amdhsa_user_sgpr_private_segment_size 0
		.amdhsa_uses_dynamic_stack 0
		.amdhsa_enable_private_segment 0
		.amdhsa_system_sgpr_workgroup_id_x 1
		.amdhsa_system_sgpr_workgroup_id_y 0
		.amdhsa_system_sgpr_workgroup_id_z 0
		.amdhsa_system_sgpr_workgroup_info 0
		.amdhsa_system_vgpr_workitem_id 0
		.amdhsa_next_free_vgpr 104
		.amdhsa_next_free_sgpr 28
		.amdhsa_accum_offset 104
		.amdhsa_reserve_vcc 0
		.amdhsa_float_round_mode_32 0
		.amdhsa_float_round_mode_16_64 0
		.amdhsa_float_denorm_mode_32 3
		.amdhsa_float_denorm_mode_16_64 3
		.amdhsa_dx10_clamp 1
		.amdhsa_ieee_mode 1
		.amdhsa_fp16_overflow 0
		.amdhsa_tg_split 0
		.amdhsa_exception_fp_ieee_invalid_op 0
		.amdhsa_exception_fp_denorm_src 0
		.amdhsa_exception_fp_ieee_div_zero 0
		.amdhsa_exception_fp_ieee_overflow 0
		.amdhsa_exception_fp_ieee_underflow 0
		.amdhsa_exception_fp_ieee_inexact 0
		.amdhsa_exception_int_div_zero 0
	.end_amdhsa_kernel

amdhsa.kernels:
  - .agpr_count:     0
    .args:
      - .offset:         0
        .size:           400
        .value_kind:     by_value
    .group_segment_fixed_size: 33280
    .kernarg_segment_align: 8
    .kernarg_segment_size: 400
    .language:       OpenCL C
    .language_version:
      - 2
      - 0
    .max_flat_workgroup_size: 256
    .name:           _Z10wt_convert7CvtJobs
    .private_segment_fixed_size: 0
    .sgpr_count:     54
    .sgpr_spill_count: 0
    .symbol:         _Z10wt_convert7CvtJobs.kd
    .uniform_work_group_size: 1
    .uses_dynamic_stack: false
    .vgpr_count:     45
    .vgpr_spill_count: 0
    .wavefront_size: 64
  - .agpr_count:     0
    .args:
      - .actual_access:  read_only
        .address_space:  global
        .offset:         0
        .size:           8
        .value_kind:     global_buffer
      - .actual_access:  read_only
        .address_space:  global
        .offset:         8
        .size:           8
        .value_kind:     global_buffer
      - .actual_access:  read_only
        .address_space:  global
        .offset:         16
        .size:           8
        .value_kind:     global_buffer
      - .actual_access:  write_only
        .address_space:  global
        .offset:         24
        .size:           8
        .value_kind:     global_buffer
      - .actual_access:  read_only
        .address_space:  global
        .offset:         32
        .size:           8
        .value_kind:     global_buffer
      - .actual_access:  read_only
        .address_space:  global
        .offset:         40
        .size:           8
        .value_kind:     global_buffer
      - .actual_access:  write_only
        .address_space:  global
        .offset:         48
        .size:           8
        .value_kind:     global_buffer
      - .offset:         56
        .size:           400
        .value_kind:     by_value
    .group_segment_fixed_size: 33280
    .kernarg_segment_align: 8
    .kernarg_segment_size: 456
    .language:       OpenCL C
    .language_version:
      - 2
      - 0
    .max_flat_workgroup_size: 256
    .name:           _Z13embed_ln_convPKiPKfS2_PfS2_S2_PDF16_7CvtJobs
    .private_segment_fixed_size: 0
    .sgpr_count:     36
    .sgpr_spill_count: 0
    .symbol:         _Z13embed_ln_convPKiPKfS2_PfS2_S2_PDF16_7CvtJobs.kd
    .uniform_work_group_size: 1
    .uses_dynamic_stack: false
    .vgpr_count:     79
    .vgpr_spill_count: 0
    .wavefront_size: 64
  - .agpr_count:     0
    .args:
      - .address_space:  global
        .offset:         0
        .size:           8
        .value_kind:     global_buffer
      - .address_space:  global
        .offset:         8
        .size:           8
        .value_kind:     global_buffer
      - .actual_access:  write_only
        .address_space:  global
        .offset:         16
        .size:           8
        .value_kind:     global_buffer
      - .actual_access:  read_only
        .address_space:  global
        .offset:         24
        .size:           8
        .value_kind:     global_buffer
      - .offset:         32
        .size:           4
        .value_kind:     by_value
      - .offset:         36
        .size:           4
        .value_kind:     by_value
      - .offset:         40
        .size:           4
        .value_kind:     by_value
    .group_segment_fixed_size: 0
    .kernarg_segment_align: 8
    .kernarg_segment_size: 44
    .language:       OpenCL C
    .language_version:
      - 2
      - 0
    .max_flat_workgroup_size: 512
    .name:           _Z17gemm_256sq_8phasePKDF16_S0_PfPKfiii
    .private_segment_fixed_size: 0
    .sgpr_count:     47
    .sgpr_spill_count: 0
    .symbol:         _Z17gemm_256sq_8phasePKDF16_S0_PfPKfiii.kd
    .uniform_work_group_size: 1
    .uses_dynamic_stack: false
    .vgpr_count:     244
    .vgpr_spill_count: 0
    .wavefront_size: 64
  - .agpr_count:     0
    .args:
      - .actual_access:  read_only
        .address_space:  global
        .offset:         0
        .size:           8
        .value_kind:     global_buffer
      - .actual_access:  read_only
        .address_space:  global
        .offset:         8
        .size:           8
        .value_kind:     global_buffer
      - .actual_access:  read_only
        .address_space:  global
        .offset:         16
        .size:           8
        .value_kind:     global_buffer
      - .actual_access:  write_only
        .address_space:  global
        .offset:         24
        .size:           8
        .value_kind:     global_buffer
      - .offset:         32
        .size:           400
        .value_kind:     by_value
    .group_segment_fixed_size: 33280
    .kernarg_segment_align: 8
    .kernarg_segment_size: 432
    .language:       OpenCL C
    .language_version:
      - 2
      - 0
    .max_flat_workgroup_size: 256
    .name:           _Z11attn_kernelPKDF16_S0_S0_PDF16_7CvtJobs
    .private_segment_fixed_size: 0
    .sgpr_count:     36
    .sgpr_spill_count: 0
    .symbol:         _Z11attn_kernelPKDF16_S0_S0_PDF16_7CvtJobs.kd
    .uniform_work_group_size: 1
    .uses_dynamic_stack: false
    .vgpr_count:     116
    .vgpr_spill_count: 0
    .wavefront_size: 64
  - .agpr_count:     0
    .args:
      - .address_space:  global
        .offset:         0
        .size:           8
        .value_kind:     global_buffer
      - .address_space:  global
        .offset:         8
        .size:           8
        .value_kind:     global_buffer
      - .offset:         16
        .size:           4
        .value_kind:     by_value
      - .offset:         20
        .size:           4
        .value_kind:     by_value
      - .offset:         24
        .size:           4
        .value_kind:     by_value
      - .actual_access:  write_only
        .address_space:  global
        .offset:         32
        .size:           8
        .value_kind:     global_buffer
      - .actual_access:  read_only
        .address_space:  global
        .offset:         40
        .size:           8
        .value_kind:     global_buffer
      - .actual_access:  read_only
        .address_space:  global
        .offset:         48
        .size:           8
        .value_kind:     global_buffer
      - .offset:         56
        .size:           4
        .value_kind:     hidden_block_count_x
      - .offset:         60
        .size:           4
        .value_kind:     hidden_block_count_y
      - .offset:         64
        .size:           4
        .value_kind:     hidden_block_count_z
      - .offset:         68
        .size:           2
        .value_kind:     hidden_group_size_x
      - .offset:         70
        .size:           2
        .value_kind:     hidden_group_size_y
      - .offset:         72
        .size:           2
        .value_kind:     hidden_group_size_z
      - .offset:         74
        .size:           2
        .value_kind:     hidden_remainder_x
      - .offset:         76
        .size:           2
        .value_kind:     hidden_remainder_y
      - .offset:         78
        .size:           2
        .value_kind:     hidden_remainder_z
      - .offset:         96
        .size:           8
        .value_kind:     hidden_global_offset_x
      - .offset:         104
        .size:           8
        .value_kind:     hidden_global_offset_y
      - .offset:         112
        .size:           8
        .value_kind:     hidden_global_offset_z
      - .offset:         120
        .size:           2
        .value_kind:     hidden_grid_dims
      - .offset:         176
        .size:           4
        .value_kind:     hidden_dynamic_lds_size
    .group_segment_fixed_size: 0
    .kernarg_segment_align: 8
    .kernarg_segment_size: 312
    .language:       OpenCL C
    .language_version:
      - 2
      - 0
    .max_flat_workgroup_size: 512
    .name:           _Z5gemm8ILi192ELi2ELi3ELi0ELi1ELi16EEvPKDF16_S1_iiiPDF16_PfPKf
    .private_segment_fixed_size: 0
    .sgpr_count:     34
    .sgpr_spill_count: 0
    .symbol:         _Z5gemm8ILi192ELi2ELi3ELi0ELi1ELi16EEvPKDF16_S1_iiiPDF16_PfPKf.kd
    .uniform_work_group_size: 1
    .uses_dynamic_stack: false
    .vgpr_count:     125
    .vgpr_spill_count: 0
    .wavefront_size: 64
  - .agpr_count:     0
    .args:
      - .address_space:  global
        .offset:         0
        .size:           8
        .value_kind:     global_buffer
      - .address_space:  global
        .offset:         8
        .size:           8
        .value_kind:     global_buffer
      - .offset:         16
        .size:           4
        .value_kind:     by_value
      - .offset:         20
        .size:           4
        .value_kind:     by_value
      - .offset:         24
        .size:           4
        .value_kind:     by_value
      - .actual_access:  write_only
        .address_space:  global
        .offset:         32
        .size:           8
        .value_kind:     global_buffer
      - .actual_access:  read_only
        .address_space:  global
        .offset:         40
        .size:           8
        .value_kind:     global_buffer
      - .actual_access:  read_only
        .address_space:  global
        .offset:         48
        .size:           8
        .value_kind:     global_buffer
      - .offset:         56
        .size:           4
        .value_kind:     hidden_block_count_x
      - .offset:         60
        .size:           4
        .value_kind:     hidden_block_count_y
      - .offset:         64
        .size:           4
        .value_kind:     hidden_block_count_z
      - .offset:         68
        .size:           2
        .value_kind:     hidden_group_size_x
      - .offset:         70
        .size:           2
        .value_kind:     hidden_group_size_y
      - .offset:         72
        .size:           2
        .value_kind:     hidden_group_size_z
      - .offset:         74
        .size:           2
        .value_kind:     hidden_remainder_x
      - .offset:         76
        .size:           2
        .value_kind:     hidden_remainder_y
      - .offset:         78
        .size:           2
        .value_kind:     hidden_remainder_z
      - .offset:         96
        .size:           8
        .value_kind:     hidden_global_offset_x
      - .offset:         104
        .size:           8
        .value_kind:     hidden_global_offset_y
      - .offset:         112
        .size:           8
        .value_kind:     hidden_global_offset_z
      - .offset:         120
        .size:           2
        .value_kind:     hidden_grid_dims
      - .offset:         176
        .size:           4
        .value_kind:     hidden_dynamic_lds_size
    .group_segment_fixed_size: 0
    .kernarg_segment_align: 8
    .kernarg_segment_size: 312
    .language:       OpenCL C
    .language_version:
      - 2
      - 0
    .max_flat_workgroup_size: 512
    .name:           _Z5gemm8ILi128ELi2ELi2ELi2ELi1ELi16EEvPKDF16_S1_iiiPDF16_PfPKf
    .private_segment_fixed_size: 0
    .sgpr_count:     30
    .sgpr_spill_count: 0
    .symbol:         _Z5gemm8ILi128ELi2ELi2ELi2ELi1ELi16EEvPKDF16_S1_iiiPDF16_PfPKf.kd
    .uniform_work_group_size: 1
    .uses_dynamic_stack: false
    .vgpr_count:     90
    .vgpr_spill_count: 0
    .wavefront_size: 64
  - .agpr_count:     0
    .args:
      - .address_space:  global
        .offset:         0
        .size:           8
        .value_kind:     global_buffer
      - .address_space:  global
        .offset:         8
        .size:           8
        .value_kind:     global_buffer
      - .offset:         16
        .size:           4
        .value_kind:     by_value
      - .offset:         20
        .size:           4
        .value_kind:     by_value
      - .offset:         24
        .size:           4
        .value_kind:     by_value
      - .actual_access:  read_only
        .address_space:  global
        .offset:         32
        .size:           8
        .value_kind:     global_buffer
      - .address_space:  global
        .offset:         40
        .size:           8
        .value_kind:     global_buffer
      - .actual_access:  read_only
        .address_space:  global
        .offset:         48
        .size:           8
        .value_kind:     global_buffer
      - .offset:         56
        .size:           4
        .value_kind:     hidden_block_count_x
      - .offset:         60
        .size:           4
        .value_kind:     hidden_block_count_y
      - .offset:         64
        .size:           4
        .value_kind:     hidden_block_count_z
      - .offset:         68
        .size:           2
        .value_kind:     hidden_group_size_x
      - .offset:         70
        .size:           2
        .value_kind:     hidden_group_size_y
      - .offset:         72
        .size:           2
        .value_kind:     hidden_group_size_z
      - .offset:         74
        .size:           2
        .value_kind:     hidden_remainder_x
      - .offset:         76
        .size:           2
        .value_kind:     hidden_remainder_y
      - .offset:         78
        .size:           2
        .value_kind:     hidden_remainder_z
      - .offset:         96
        .size:           8
        .value_kind:     hidden_global_offset_x
      - .offset:         104
        .size:           8
        .value_kind:     hidden_global_offset_y
      - .offset:         112
        .size:           8
        .value_kind:     hidden_global_offset_z
      - .offset:         120
        .size:           2
        .value_kind:     hidden_grid_dims
      - .offset:         176
        .size:           4
        .value_kind:     hidden_dynamic_lds_size
    .group_segment_fixed_size: 0
    .kernarg_segment_align: 8
    .kernarg_segment_size: 312
    .language:       OpenCL C
    .language_version:
      - 2
      - 0
    .max_flat_workgroup_size: 512
    .name:           _Z5gemm8ILi64ELi4ELi6ELi1ELi1ELi16EEvPKDF16_S1_iiiPDF16_PfPKf
    .private_segment_fixed_size: 0
    .sgpr_count:     34
    .sgpr_spill_count: 0
    .symbol:         _Z5gemm8ILi64ELi4ELi6ELi1ELi1ELi16EEvPKDF16_S1_iiiPDF16_PfPKf.kd
    .uniform_work_group_size: 1
    .uses_dynamic_stack: false
    .vgpr_count:     104
    .vgpr_spill_count: 0
    .wavefront_size: 64
  - .agpr_count:     0
    .args:
      - .address_space:  global
        .offset:         0
        .size:           8
        .value_kind:     global_buffer
      - .address_space:  global
        .offset:         8
        .size:           8
        .value_kind:     global_buffer
      - .offset:         16
        .size:           4
        .value_kind:     by_value
      - .offset:         20
        .size:           4
        .value_kind:     by_value
      - .offset:         24
        .size:           4
        .value_kind:     by_value
      - .actual_access:  write_only
        .address_space:  global
        .offset:         32
        .size:           8
        .value_kind:     global_buffer
      - .actual_access:  read_only
        .address_space:  global
        .offset:         40
        .size:           8
        .value_kind:     global_buffer
      - .actual_access:  read_only
        .address_space:  global
        .offset:         48
        .size:           8
        .value_kind:     global_buffer
    .group_segment_fixed_size: 0
    .kernarg_segment_align: 8
    .kernarg_segment_size: 56
    .language:       OpenCL C
    .language_version:
      - 2
      - 0
    .max_flat_workgroup_size: 512
    .name:           _Z5gemm8ILi128ELi2ELi4ELi4ELi2ELi32EEvPKDF16_S1_iiiPDF16_PfPKf
    .private_segment_fixed_size: 0
    .sgpr_count:     38
    .sgpr_spill_count: 0
    .symbol:         _Z5gemm8ILi128ELi2ELi4ELi4ELi2ELi32EEvPKDF16_S1_iiiPDF16_PfPKf.kd
    .uniform_work_group_size: 1
    .uses_dynamic_stack: false
    .vgpr_count:     107
    .vgpr_spill_count: 0
    .wavefront_size: 64
  - .agpr_count:     0
    .args:
      - .actual_access:  read_only
        .address_space:  global
        .offset:         0
        .size:           8
        .value_kind:     global_buffer
      - .actual_access:  read_only
        .address_space:  global
        .offset:         8
        .size:           8
        .value_kind:     global_buffer
      - .actual_access:  read_only
        .address_space:  global
        .offset:         16
        .size:           8
        .value_kind:     global_buffer
      - .address_space:  global
        .offset:         24
        .size:           8
        .value_kind:     global_buffer
      - .actual_access:  read_only
        .address_space:  global
        .offset:         32
        .size:           8
        .value_kind:     global_buffer
      - .actual_access:  read_only
        .address_space:  global
        .offset:         40
        .size:           8
        .value_kind:     global_buffer
      - .actual_access:  write_only
        .address_space:  global
        .offset:         48
        .size:           8
        .value_kind:     global_buffer
    .group_segment_fixed_size: 0
    .kernarg_segment_align: 8
    .kernarg_segment_size: 56
    .language:       OpenCL C
    .language_version:
      - 2
      - 0
    .max_flat_workgroup_size: 256
    .name:           _Z9ln_kernelILi2EEvPKiPKfS3_PfS3_S3_PDF16_
    .private_segment_fixed_size: 0
    .sgpr_count:     18
    .sgpr_spill_count: 0
    .symbol:         _Z9ln_kernelILi2EEvPKiPKfS3_PfS3_S3_PDF16_.kd
    .uniform_work_group_size: 1
    .uses_dynamic_stack: false
    .vgpr_count:     58
    .vgpr_spill_count: 0
    .wavefront_size: 64
  - .agpr_count:     0
    .args:
      - .actual_access:  read_only
        .address_space:  global
        .offset:         0
        .size:           8
        .value_kind:     global_buffer
      - .actual_access:  read_only
        .address_space:  global
        .offset:         8
        .size:           8
        .value_kind:     global_buffer
      - .actual_access:  read_only
        .address_space:  global
        .offset:         16
        .size:           8
        .value_kind:     global_buffer
      - .actual_access:  read_only
        .address_space:  global
        .offset:         24
        .size:           8
        .value_kind:     global_buffer
      - .actual_access:  read_only
        .address_space:  global
        .offset:         32
        .size:           8
        .value_kind:     global_buffer
      - .actual_access:  read_only
        .address_space:  global
        .offset:         40
        .size:           8
        .value_kind:     global_buffer
      - .actual_access:  write_only
        .address_space:  global
        .offset:         48
        .size:           8
        .value_kind:     global_buffer
    .group_segment_fixed_size: 0
    .kernarg_segment_align: 8
    .kernarg_segment_size: 56
    .language:       OpenCL C
    .language_version:
      - 2
      - 0
    .max_flat_workgroup_size: 256
    .name:           _Z9ln_kernelILi0EEvPKiPKfS3_PfS3_S3_PDF16_
    .private_segment_fixed_size: 0
    .sgpr_count:     18
    .sgpr_spill_count: 0
    .symbol:         _Z9ln_kernelILi0EEvPKiPKfS3_PfS3_S3_PDF16_.kd
    .uniform_work_group_size: 1
    .uses_dynamic_stack: false
    .vgpr_count:     60
    .vgpr_spill_count: 0
    .wavefront_size: 64
  - .agpr_count:     0
    .args:
      - .actual_access:  read_only
        .address_space:  global
        .offset:         0
        .size:           8
        .value_kind:     global_buffer
      - .actual_access:  read_only
        .address_space:  global
        .offset:         8
        .size:           8
        .value_kind:     global_buffer
      - .actual_access:  read_only
        .address_space:  global
        .offset:         16
        .size:           8
        .value_kind:     global_buffer
      - .actual_access:  read_only
        .address_space:  global
        .offset:         24
        .size:           8
        .value_kind:     global_buffer
      - .actual_access:  read_only
        .address_space:  global
        .offset:         32
        .size:           8
        .value_kind:     global_buffer
      - .actual_access:  read_only
        .address_space:  global
        .offset:         40
        .size:           8
        .value_kind:     global_buffer
      - .actual_access:  write_only
        .address_space:  global
        .offset:         48
        .size:           8
        .value_kind:     global_buffer
    .group_segment_fixed_size: 0
    .kernarg_segment_align: 8
    .kernarg_segment_size: 56
    .language:       OpenCL C
    .language_version:
      - 2
      - 0
    .max_flat_workgroup_size: 256
    .name:           _Z9ln_kernelILi4EEvPKiPKfS3_PfS3_S3_PDF16_
    .private_segment_fixed_size: 0
    .sgpr_count:     18
    .sgpr_spill_count: 0
    .symbol:         _Z9ln_kernelILi4EEvPKiPKfS3_PfS3_S3_PDF16_.kd
    .uniform_work_group_size: 1
    .uses_dynamic_stack: false
    .vgpr_count:     64
    .vgpr_spill_count: 0
    .wavefront_size: 64
